# v027 plus per-CU start stagger in A6 phase
# baseline (speedup 1.0000x reference)
.Lstg_a6_done:
	v_readlane_b32 s8, v254, 3
	s_mov_b64 s[4:5], s[74:75]
	v_mov_b32_e32 v14, v0
	v_readlane_b32 s9, v254, 4
	s_load_dword s44, s[8:9], 0x0
	s_and_b64 s[8:9], s[64:65], exec
	s_movk_i32 s8, 0x80
	s_cselect_b32 s46, s8, 0x84
	v_readlane_b32 s45, v254, 0
	s_lshl_b32 s36, s46, 2
	s_waitcnt lgkmcnt(0)
	s_cmp_ge_i32 s45, s36
	v_readfirstlane_b32 s16, v14
	s_cbranch_scc1 .LBB0_1132
	v_lshlrev_b32_e32 v1, 4, v14
	v_add_u32_e32 v2, 0x2000, v1
	v_ashrrev_i32_e32 v4, 31, v2
	v_lshrrev_b32_e32 v4, 22, v4
	v_add_u32_e32 v4, v2, v4
	v_ashrrev_i32_e32 v12, 10, v4
	s_load_dwordx2 s[4:5], s[4:5], 0xd8
	v_mul_i32_i24_e32 v4, 0x400, v12
	v_sub_u32_e32 v2, v2, v4
	v_lshrrev_b32_e32 v4, 4, v2
	v_bitop3_b32 v2, v4, v2, 32 bitop3:0x6c
	v_ashrrev_i32_e32 v4, 31, v2
	v_readlane_b32 s8, v255, 20
	s_waitcnt lgkmcnt(0)
	s_add_u32 s47, s4, 0x18800000
	v_lshrrev_b32_e32 v4, 26, v4
	s_mul_i32 s8, s8, 0xc10000
	s_addc_u32 s48, s5, 0
	v_add_u32_e32 v4, v2, v4
	v_lshlrev_b32_e32 v5, 3, v12
	s_add_u32 s8, s4, s8
	v_ashrrev_i32_e32 v13, 6, v4
	v_and_b32_e32 v5, -16, v5
	s_addc_u32 s9, s5, 0
	v_add_u32_e32 v5, v13, v5
	s_add_u32 s49, s8, 0x1010000
	v_and_b32_e32 v6, 3, v13
	s_mov_b32 s8, 0x3fffe0
	v_lshrrev_b32_e32 v7, 2, v5
	v_lshlrev_b32_e32 v8, 1, v5
	v_and_b32_e32 v4, 0xc0, v4
	v_and_or_b32 v6, v5, s8, v6
	v_and_b32_e32 v7, 4, v7
	v_and_b32_e32 v8, 24, v8
	v_sub_u32_e32 v2, v2, v4
	v_or3_b32 v6, v6, v7, v8
	v_lshlrev_b32_e32 v7, 5, v12
	v_ashrrev_i16_sdwa v2, v243, sext(v2) dst_sel:DWORD dst_unused:UNUSED_PAD src0_sel:DWORD src1_sel:BYTE_0
	v_and_b32_e32 v7, 32, v7
	v_bfe_i32 v15, v2, 0, 16
	v_add_lshl_u32 v2, v7, v15, 1
	v_lshl_add_u32 v140, v6, 10, v2
	v_lshl_add_u32 v142, v5, 10, v2
	v_bfe_i32 v2, v14, 27, 1
	v_lshrrev_b32_e32 v2, 22, v2
	v_add_u32_e32 v2, v1, v2
	v_and_b32_e32 v2, 0xfffffc00, v2
	v_sub_u32_e32 v1, v1, v2
	v_lshrrev_b32_e32 v2, 4, v1
	v_ashrrev_i32_e32 v4, 31, v14
	v_bitop3_b32 v1, v2, v1, 32 bitop3:0x6c
	v_lshrrev_b32_e32 v4, 26, v4
	v_ashrrev_i32_e32 v2, 31, v1
	v_add_u32_e32 v4, v14, v4
	v_lshrrev_b32_e32 v2, 26, v2
	v_ashrrev_i32_e32 v17, 6, v4
	v_add_u32_e32 v2, v1, v2
	v_lshlrev_b32_e32 v4, 3, v17
	v_ashrrev_i32_e32 v16, 6, v2
	v_and_b32_e32 v4, -16, v4
	s_addc_u32 s50, s9, 0
	v_add_u32_e32 v4, v16, v4
	v_and_b32_e32 v5, 3, v16
	s_ashr_i32 s53, s45, 31
	v_and_or_b32 v5, v4, s8, v5
	s_lshr_b32 s8, s53, 29
	s_add_i32 s8, s45, s8
	s_ashr_i32 s17, s16, 6
	s_lshr_b32 s52, s46, 1
	s_ashr_i32 s9, s8, 3
	s_and_b32 s8, s8, -8
	s_ashr_i32 s18, s16, 8
	s_lshl_b32 s51, s17, 10
	s_sub_i32 s8, s45, s8
	s_or_b32 s54, s52, 1
	s_cmp_lt_i32 s8, 0
	s_cselect_b32 s10, s54, s52
	s_mul_i32 s8, s8, s10
	s_add_i32 s8, s8, s9
	s_ashr_i32 s9, s8, 31
	s_lshr_b32 s9, s9, 27
	s_add_i32 s9, s8, s9
	v_lshrrev_b32_e32 v6, 2, v4
	v_lshlrev_b32_e32 v7, 1, v4
	v_and_b32_e32 v2, 0xc0, v2
	s_ashr_i32 s10, s9, 5
	v_and_b32_e32 v6, 4, v6
	v_and_b32_e32 v7, 24, v7
	v_sub_u32_e32 v1, v1, v2
	s_andn2_b32 s9, s9, 31
	s_lshl_b32 s12, s10, 3
	v_or3_b32 v5, v5, v6, v7
	v_lshlrev_b32_e32 v6, 5, v17
	v_ashrrev_i16_sdwa v1, v243, sext(v1) dst_sel:DWORD dst_unused:UNUSED_PAD src0_sel:DWORD src1_sel:BYTE_0
	s_sub_i32 s11, s8, s9
	s_sub_i32 s8, s46, s12
	v_and_b32_e32 v6, 32, v6
	v_bfe_i32 v18, v1, 0, 16
	s_min_u32 s13, s8, 8
	v_add_lshl_u32 v1, v6, v18, 1
	v_cvt_f32_ubyte0_e32 v6, s13
	v_lshl_add_u32 v2, v5, 10, v1
	v_cvt_f32_i32_e32 v5, s11
	v_rcp_iflag_f32_e32 v7, v6
	v_lshl_add_u32 v144, v4, 10, v1
	s_ashr_i32 s8, s11, 30
	s_or_b32 s10, s8, 1
	v_mul_f32_e32 v1, v5, v7
	v_trunc_f32_e32 v1, v1
	v_fma_f32 v4, -v1, v6, v5
	v_cvt_i32_f32_e32 v1, v1
	v_cmp_ge_f32_e64 s[8:9], |v4|, v6
	s_and_b64 s[8:9], s[8:9], exec
	s_cselect_b32 s8, s10, 0
	v_readfirstlane_b32 s9, v1
	s_add_i32 s10, s9, s8
	s_mul_i32 s8, s10, s13
	s_sub_i32 s8, s11, s8
	s_sext_i32_i8 s8, s8
	s_add_i32 s12, s12, s8
	s_ashr_i32 s8, s12, 5
	s_add_i32 s11, s8, 1
	s_and_b64 s[8:9], s[64:65], exec
	s_cselect_b32 s8, s11, 0
	s_add_i32 s40, s8, s12
	s_ashr_i32 s41, s40, 31
	s_bfe_i64 s[12:13], s[10:11], 0x80000
	s_lshl_b64 s[8:9], s[40:41], 18
	s_lshl_b64 s[12:13], s[12:13], 18
	s_add_u32 s38, s49, s12
	s_addc_u32 s39, s50, s13
	s_add_i32 s41, s51, 0
	s_add_i32 m0, s41, 0x10000
	v_mov_b32_e32 v141, v3
	global_load_lds_dwordx4 v2, s[38:39]
	s_add_i32 m0, s41, 0x12000
	s_add_u32 s12, s38, 0x20000
	global_load_lds_dwordx4 v140, s[38:39]
	s_addc_u32 s13, s39, 0
	s_add_i32 m0, s41, 0x14000
	v_mov_b32_e32 v145, v3
	global_load_lds_dwordx4 v2, s[12:13]
	s_add_i32 m0, s41, 0x16000
	s_add_u32 s34, s47, s8
	s_addc_u32 s35, s48, s9
	s_add_i32 s55, s41, 0x2000
	global_load_lds_dwordx4 v140, s[12:13]
	s_mov_b32 m0, s41
	s_add_u32 s8, s34, 0x20000
	global_load_lds_dwordx4 v144, s[34:35]
	s_mov_b32 m0, s55
	s_addc_u32 s9, s35, 0
	s_add_i32 s60, s41, 0x4000
	global_load_lds_dwordx4 v142, s[34:35]
	s_mov_b32 m0, s60
	s_add_i32 s61, s41, 0x6000
	global_load_lds_dwordx4 v144, s[8:9]
	s_mov_b32 m0, s61
	v_mov_b32_e32 v143, v3
	global_load_lds_dwordx4 v142, s[8:9]
	s_cmp_eq_u32 s18, 1
	v_lshl_add_u64 v[10:11], s[38:39], 0, v[2:3]
	v_lshl_add_u64 v[8:9], s[38:39], 0, v[140:141]
	v_lshl_add_u64 v[4:5], s[34:35], 0, v[144:145]
	s_cselect_b64 s[8:9], -1, 0
	s_cmp_lg_u32 s18, 1
	v_lshl_add_u64 v[6:7], s[34:35], 0, v[142:143]
	s_cbranch_scc1 .LBB0_1113
	s_barrier
